# P7 token-list tail loop: the 8 loads of a 4-row trip issued together behind one wait (was 4 serial load-wait-store chains)
# baseline (speedup 1.0000x reference)
; template <bool FAST>
; __device__ __forceinline__ void p7_route_t(Frame& F, const bool do_route) {
;     ...
;     for (int it = 0; it < NIT; ++it) { const int row = FAST ? (F.bx * NIT + it) * 8 + F.wave : gw + it * NGW;
;         if (row < M_LAT && F.lane < TOPK) { const int e = tok_e[row * TOPK + F.lane]; const int idx = (int)lcnt[32 + e] + tok_rank[row * TOPK + F.lane];
;             tok_rank[row * TOPK + F.lane] = idx; elist[((size_t)e * RR + rep) * RCAP + idx] = row; } }
.LBB0_843:
	s_add_i32 s9, s7, -24
	s_cmpk_lt_i32 s9, 0x4000
	s_cselect_b64 s[2:3], -1, 0
	s_and_b64 s[10:11], s[2:3], s[4:5]
	s_and_saveexec_b64 s[2:3], s[10:11]
	v_add_u32_e32 v4, 0xffffffa0, v2
	v_ashrrev_i32_e32 v5, 31, v4
	v_lshlrev_b64 v[4:5], 2, v[4:5]
	v_lshl_add_u64 v[6:7], s[82:83], 0, v[4:5]
	global_load_dword v240, v[6:7], off
	v_lshl_add_u64 v[238:239], s[86:87], 0, v[4:5]
	global_load_dword v241, v[238:239], off
	s_or_b64 exec, exec, s[2:3]
	s_add_i32 s9, s7, -16
	s_cmpk_lt_i32 s9, 0x4000
	s_cselect_b64 s[2:3], -1, 0
	s_and_b64 s[10:11], s[2:3], s[4:5]
	s_and_saveexec_b64 s[2:3], s[10:11]
	v_add_u32_e32 v4, 0xffffffc0, v2
	v_ashrrev_i32_e32 v5, 31, v4
	v_lshlrev_b64 v[4:5], 2, v[4:5]
	v_lshl_add_u64 v[6:7], s[82:83], 0, v[4:5]
	global_load_dword v244, v[6:7], off
	v_lshl_add_u64 v[242:243], s[86:87], 0, v[4:5]
	global_load_dword v245, v[242:243], off
	s_or_b64 exec, exec, s[2:3]
	s_add_i32 s9, s7, -8
	s_cmpk_lt_i32 s9, 0x4000
	s_cselect_b64 s[2:3], -1, 0
	s_and_b64 s[10:11], s[2:3], s[4:5]
	s_and_saveexec_b64 s[2:3], s[10:11]
	v_add_u32_e32 v4, 0xffffffe0, v2
	v_ashrrev_i32_e32 v5, 31, v4
	v_lshlrev_b64 v[4:5], 2, v[4:5]
	v_lshl_add_u64 v[6:7], s[82:83], 0, v[4:5]
	global_load_dword v248, v[6:7], off
	v_lshl_add_u64 v[246:247], s[86:87], 0, v[4:5]
	global_load_dword v249, v[246:247], off
	s_or_b64 exec, exec, s[2:3]
	s_add_i32 s9, s7, 0
	s_cmpk_lt_i32 s9, 0x4000
	s_cselect_b64 s[2:3], -1, 0
	s_and_b64 s[10:11], s[2:3], s[4:5]
	s_and_saveexec_b64 s[2:3], s[10:11]
	v_add_u32_e32 v4, 0, v2
	v_ashrrev_i32_e32 v5, 31, v4
	v_lshlrev_b64 v[4:5], 2, v[4:5]
	v_lshl_add_u64 v[6:7], s[82:83], 0, v[4:5]
	global_load_dword v252, v[6:7], off
	v_lshl_add_u64 v[250:251], s[86:87], 0, v[4:5]
	global_load_dword v253, v[250:251], off
	s_or_b64 exec, exec, s[2:3]
	s_waitcnt vmcnt(0)
	s_add_i32 s9, s7, -24
	s_cmpk_lt_i32 s9, 0x4000
	s_cselect_b64 s[2:3], -1, 0
	s_and_b64 s[10:11], s[2:3], s[4:5]
	s_and_saveexec_b64 s[2:3], s[10:11]
	v_lshl_add_u32 v7, v240, 2, 0
	ds_read_b32 v8, v7 offset:128
	v_mov_b32_e32 v6, v240
	v_ashrrev_i32_e32 v7, 31, v240
	v_lshlrev_b64 v[6:7], 17, v[6:7]
	v_lshl_add_u64 v[6:7], s[0:1], 0, v[6:7]
	s_waitcnt lgkmcnt(0)
	v_add_u32_e32 v8, v241, v8
	v_ashrrev_i32_e32 v9, 31, v8
	global_store_dword v[238:239], v8, off
	v_lshl_add_u64 v[4:5], v[8:9], 2, v[6:7]
	v_mov_b32_e32 v3, s9
	global_store_dword v[4:5], v3, off
	s_or_b64 exec, exec, s[2:3]
	s_add_i32 s9, s7, -16
	s_cmpk_lt_i32 s9, 0x4000
	s_cselect_b64 s[2:3], -1, 0
	s_and_b64 s[10:11], s[2:3], s[4:5]
	s_and_saveexec_b64 s[2:3], s[10:11]
	v_lshl_add_u32 v7, v244, 2, 0
	ds_read_b32 v8, v7 offset:128
	v_mov_b32_e32 v6, v244
	v_ashrrev_i32_e32 v7, 31, v244
	v_lshlrev_b64 v[6:7], 17, v[6:7]
	v_lshl_add_u64 v[6:7], s[0:1], 0, v[6:7]
	s_waitcnt lgkmcnt(0)
	v_add_u32_e32 v8, v245, v8
	v_ashrrev_i32_e32 v9, 31, v8
	global_store_dword v[242:243], v8, off
	v_lshl_add_u64 v[4:5], v[8:9], 2, v[6:7]
	v_mov_b32_e32 v3, s9
	global_store_dword v[4:5], v3, off
	s_or_b64 exec, exec, s[2:3]
	s_add_i32 s9, s7, -8
	s_cmpk_lt_i32 s9, 0x4000
	s_cselect_b64 s[2:3], -1, 0
	s_and_b64 s[10:11], s[2:3], s[4:5]
	s_and_saveexec_b64 s[2:3], s[10:11]
	v_lshl_add_u32 v7, v248, 2, 0
	ds_read_b32 v8, v7 offset:128
	v_mov_b32_e32 v6, v248
	v_ashrrev_i32_e32 v7, 31, v248
	v_lshlrev_b64 v[6:7], 17, v[6:7]
	v_lshl_add_u64 v[6:7], s[0:1], 0, v[6:7]
	s_waitcnt lgkmcnt(0)
	v_add_u32_e32 v8, v249, v8
	v_ashrrev_i32_e32 v9, 31, v8
	global_store_dword v[246:247], v8, off
	v_lshl_add_u64 v[4:5], v[8:9], 2, v[6:7]
	v_mov_b32_e32 v3, s9
	global_store_dword v[4:5], v3, off
	s_or_b64 exec, exec, s[2:3]
	s_add_i32 s9, s7, 0
	s_cmpk_lt_i32 s9, 0x4000
	s_cselect_b64 s[2:3], -1, 0
	s_and_b64 s[10:11], s[2:3], s[4:5]
	s_and_saveexec_b64 s[2:3], s[10:11]
	v_lshl_add_u32 v7, v252, 2, 0
	ds_read_b32 v8, v7 offset:128
	v_mov_b32_e32 v6, v252
	v_ashrrev_i32_e32 v7, 31, v252
	v_lshlrev_b64 v[6:7], 17, v[6:7]
	v_lshl_add_u64 v[6:7], s[0:1], 0, v[6:7]
	s_waitcnt lgkmcnt(0)
	v_add_u32_e32 v8, v253, v8
	v_ashrrev_i32_e32 v9, 31, v8
	global_store_dword v[250:251], v8, off
	v_lshl_add_u64 v[4:5], v[8:9], 2, v[6:7]
	v_mov_b32_e32 v3, s9
	global_store_dword v[4:5], v3, off
	s_or_b64 exec, exec, s[2:3]
	s_branch .LBB0_842
